# g28: g22 + converted fp8 MoE weights (402 MB, next read in P6/P7) stored non-temporal in P3
# speedup vs baseline: 1.0053x; 1.0053x over previous
.LBB0_306:
	ds_read2st64_b32 v[86:87], v79 offset1:2
	ds_read2st64_b32 v[88:89], v79 offset0:4 offset1:6
	ds_read2st64_b32 v[90:91], v79 offset0:8 offset1:10
	s_lshl_b64 s[16:17], s[8:9], 11
	s_add_u32 s8, s10, s16
	s_waitcnt lgkmcnt(2)
	v_mul_f32_e32 v85, 0x42800000, v86
	v_mul_f32_e32 v87, 0x42800000, v87
	v_mov_b32_e32 v86, v67
	v_cvt_pk_fp8_f32 v86, v85, v87
	s_waitcnt lgkmcnt(1)
	v_mul_f32_e32 v85, 0x42800000, v88
	v_mul_f32_e32 v92, 0x42800000, v89
	s_waitcnt lgkmcnt(0)
	v_mul_f32_e32 v90, 0x42800000, v90
	v_mul_f32_e32 v91, 0x42800000, v91
	ds_read2st64_b32 v[88:89], v79 offset0:12 offset1:14
	v_mov_b32_e32 v87, v67
	v_cvt_pk_fp8_f32 v87, v90, v91
	ds_read2st64_b32 v[90:91], v79 offset0:16 offset1:18
	v_cvt_pk_fp8_f32 v86, v85, v92 op_sel:[0,0,1]
	s_waitcnt lgkmcnt(1)
	v_mul_f32_e32 v85, 0x42800000, v88
	v_mul_f32_e32 v88, 0x42800000, v89
	ds_read2st64_b32 v[92:93], v79 offset0:20 offset1:22
	v_cvt_pk_fp8_f32 v87, v85, v88 op_sel:[0,0,1]
	s_waitcnt lgkmcnt(1)
	v_mul_f32_e32 v85, 0x42800000, v90
	v_mul_f32_e32 v89, 0x42800000, v91
	v_mov_b32_e32 v88, v67
	ds_read2st64_b32 v[90:91], v79 offset0:24 offset1:26
	v_cvt_pk_fp8_f32 v88, v85, v89
	s_waitcnt lgkmcnt(1)
	v_mul_f32_e32 v85, 0x42800000, v92
	v_mul_f32_e32 v89, 0x42800000, v93
	ds_read2st64_b32 v[92:93], v79 offset0:28 offset1:30
	v_cvt_pk_fp8_f32 v88, v85, v89 op_sel:[0,0,1]
	s_waitcnt lgkmcnt(1)
	v_mul_f32_e32 v85, 0x42800000, v90
	v_mul_f32_e32 v90, 0x42800000, v91
	v_mov_b32_e32 v89, v67
	v_cvt_pk_fp8_f32 v89, v85, v90
	s_addc_u32 s11, s11, s17
	s_add_u32 s10, s8, s24
	s_addc_u32 s11, s11, 0
	s_waitcnt lgkmcnt(0)
	v_mul_f32_e32 v85, 0x42800000, v92
	v_mul_f32_e32 v92, 0x42800000, v93
	ds_read2st64_b32 v[90:91], v80 offset1:2
	v_cvt_pk_fp8_f32 v89, v85, v92 op_sel:[0,0,1]
	v_lshl_add_u64 v[92:93], s[10:11], 0, v[70:71]
	v_lshl_add_u64 v[94:95], v[92:93], 0, v[68:69]
	ds_read2st64_b32 v[92:93], v80 offset0:4 offset1:6
	ds_read2st64_b32 v[96:97], v80 offset0:8 offset1:10
	s_waitcnt lgkmcnt(2)
	v_mul_f32_e32 v85, 0x42800000, v90
	v_mul_f32_e32 v91, 0x42800000, v91
	v_mov_b32_e32 v90, v67
	v_cvt_pk_fp8_f32 v90, v85, v91
	s_waitcnt lgkmcnt(1)
	v_mul_f32_e32 v85, 0x42800000, v92
	v_mul_f32_e32 v98, 0x42800000, v93
	s_waitcnt lgkmcnt(0)
	v_mul_f32_e32 v96, 0x42800000, v96
	v_mul_f32_e32 v97, 0x42800000, v97
	ds_read2st64_b32 v[92:93], v80 offset0:12 offset1:14
	v_mov_b32_e32 v91, v67
	v_cvt_pk_fp8_f32 v91, v96, v97
	ds_read2st64_b32 v[96:97], v80 offset0:16 offset1:18
	v_cvt_pk_fp8_f32 v90, v85, v98 op_sel:[0,0,1]
	s_waitcnt lgkmcnt(1)
	v_mul_f32_e32 v85, 0x42800000, v92
	v_mul_f32_e32 v92, 0x42800000, v93
	ds_read2st64_b32 v[98:99], v80 offset0:20 offset1:22
	v_cvt_pk_fp8_f32 v91, v85, v92 op_sel:[0,0,1]
	s_waitcnt lgkmcnt(1)
	v_mul_f32_e32 v85, 0x42800000, v96
	v_mul_f32_e32 v93, 0x42800000, v97
	ds_read2st64_b32 v[96:97], v80 offset0:24 offset1:26
	v_mov_b32_e32 v92, v67
	v_cvt_pk_fp8_f32 v92, v85, v93
	s_waitcnt lgkmcnt(1)
	v_mul_f32_e32 v85, 0x42800000, v98
	v_mul_f32_e32 v100, 0x42800000, v99
	ds_read2st64_b32 v[98:99], v80 offset0:28 offset1:30
	s_waitcnt lgkmcnt(1)
	v_mul_f32_e32 v96, 0x42800000, v96
	v_mul_f32_e32 v97, 0x42800000, v97
	v_mov_b32_e32 v93, v67
	v_cvt_pk_fp8_f32 v93, v96, v97
	v_cvt_pk_fp8_f32 v92, v85, v100 op_sel:[0,0,1]
	s_waitcnt lgkmcnt(0)
	v_mul_f32_e32 v85, 0x42800000, v98
	v_mul_f32_e32 v96, 0x42800000, v99
	v_cvt_pk_fp8_f32 v93, v85, v96 op_sel:[0,0,1]
	global_store_dwordx4 v[94:95], v[86:89], off nt
	ds_read2st64_b32 v[96:97], v81 offset1:2
	ds_read2st64_b32 v[88:89], v81 offset0:4 offset1:6
	v_lshl_add_u64 v[86:87], s[10:11], 0, v[72:73]
	v_lshl_add_u64 v[86:87], v[86:87], 0, v[68:69]
	global_store_dwordx4 v[86:87], v[90:93], off nt
	ds_read2st64_b32 v[90:91], v81 offset0:8 offset1:10
	s_waitcnt lgkmcnt(2)
	v_mul_f32_e32 v85, 0x42800000, v96
	v_mul_f32_e32 v87, 0x42800000, v97
	v_mov_b32_e32 v86, v67
	v_cvt_pk_fp8_f32 v86, v85, v87
	s_waitcnt lgkmcnt(1)
	v_mul_f32_e32 v85, 0x42800000, v88
	v_mul_f32_e32 v92, 0x42800000, v89
	s_waitcnt lgkmcnt(0)
	v_mul_f32_e32 v90, 0x42800000, v90
	v_mul_f32_e32 v91, 0x42800000, v91
	ds_read2st64_b32 v[88:89], v81 offset0:12 offset1:14
	v_mov_b32_e32 v87, v67
	v_cvt_pk_fp8_f32 v87, v90, v91
	ds_read2st64_b32 v[90:91], v81 offset0:16 offset1:18
	v_cvt_pk_fp8_f32 v86, v85, v92 op_sel:[0,0,1]
	s_waitcnt lgkmcnt(1)
	v_mul_f32_e32 v85, 0x42800000, v88
	v_mul_f32_e32 v88, 0x42800000, v89
	ds_read2st64_b32 v[92:93], v81 offset0:20 offset1:22
	v_cvt_pk_fp8_f32 v87, v85, v88 op_sel:[0,0,1]
	s_waitcnt lgkmcnt(1)
	v_mul_f32_e32 v85, 0x42800000, v90
	v_mul_f32_e32 v89, 0x42800000, v91
	v_mov_b32_e32 v88, v67
	ds_read2st64_b32 v[90:91], v81 offset0:24 offset1:26
	v_cvt_pk_fp8_f32 v88, v85, v89
	s_waitcnt lgkmcnt(1)
	v_mul_f32_e32 v85, 0x42800000, v92
	v_mul_f32_e32 v89, 0x42800000, v93
	ds_read2st64_b32 v[92:93], v81 offset0:28 offset1:30
	v_cvt_pk_fp8_f32 v88, v85, v89 op_sel:[0,0,1]
	s_waitcnt lgkmcnt(1)
	v_mul_f32_e32 v85, 0x42800000, v90
	v_mul_f32_e32 v90, 0x42800000, v91
	v_mov_b32_e32 v89, v67
	v_cvt_pk_fp8_f32 v89, v85, v90
	s_waitcnt lgkmcnt(0)
	v_mul_f32_e32 v85, 0x42800000, v92
	v_mul_f32_e32 v92, 0x42800000, v93
	ds_read2st64_b32 v[90:91], v82 offset1:2
	v_cvt_pk_fp8_f32 v89, v85, v92 op_sel:[0,0,1]
	v_lshl_add_u64 v[92:93], s[10:11], 0, v[74:75]
	v_lshl_add_u64 v[94:95], v[92:93], 0, v[68:69]
	ds_read2st64_b32 v[92:93], v82 offset0:4 offset1:6
	ds_read2st64_b32 v[96:97], v82 offset0:8 offset1:10
	s_waitcnt lgkmcnt(2)
	v_mul_f32_e32 v85, 0x42800000, v90
	v_mul_f32_e32 v91, 0x42800000, v91
	v_mov_b32_e32 v90, v67
	v_cvt_pk_fp8_f32 v90, v85, v91
	s_waitcnt lgkmcnt(1)
	v_mul_f32_e32 v85, 0x42800000, v92
	v_mul_f32_e32 v98, 0x42800000, v93
	s_waitcnt lgkmcnt(0)
	v_mul_f32_e32 v96, 0x42800000, v96
	v_mul_f32_e32 v97, 0x42800000, v97
	ds_read2st64_b32 v[92:93], v82 offset0:12 offset1:14
	v_mov_b32_e32 v91, v67
	v_cvt_pk_fp8_f32 v91, v96, v97
	ds_read2st64_b32 v[96:97], v82 offset0:16 offset1:18
	v_cvt_pk_fp8_f32 v90, v85, v98 op_sel:[0,0,1]
	s_waitcnt lgkmcnt(1)
	v_mul_f32_e32 v85, 0x42800000, v92
	v_mul_f32_e32 v92, 0x42800000, v93
	ds_read2st64_b32 v[98:99], v82 offset0:20 offset1:22
	v_cvt_pk_fp8_f32 v91, v85, v92 op_sel:[0,0,1]
	s_waitcnt lgkmcnt(1)
	v_mul_f32_e32 v85, 0x42800000, v96
	v_mul_f32_e32 v93, 0x42800000, v97
	ds_read2st64_b32 v[96:97], v82 offset0:24 offset1:26
	v_mov_b32_e32 v92, v67
	v_cvt_pk_fp8_f32 v92, v85, v93
	s_waitcnt lgkmcnt(1)
	v_mul_f32_e32 v85, 0x42800000, v98
	v_mul_f32_e32 v100, 0x42800000, v99
	ds_read2st64_b32 v[98:99], v82 offset0:28 offset1:30
	s_waitcnt lgkmcnt(1)
	v_mul_f32_e32 v96, 0x42800000, v96
	v_mul_f32_e32 v97, 0x42800000, v97
	v_mov_b32_e32 v93, v67
	v_cvt_pk_fp8_f32 v93, v96, v97
	v_cvt_pk_fp8_f32 v92, v85, v100 op_sel:[0,0,1]
	s_waitcnt lgkmcnt(0)
	v_mul_f32_e32 v85, 0x42800000, v98
	v_mul_f32_e32 v96, 0x42800000, v99
	v_cvt_pk_fp8_f32 v93, v85, v96 op_sel:[0,0,1]
	global_store_dwordx4 v[94:95], v[86:89], off nt
	s_andn2_b64 vcc, exec, s[6:7]
	s_mov_b32 s8, s25
	v_lshl_add_u64 v[86:87], s[10:11], 0, v[76:77]
	v_lshl_add_u64 v[86:87], v[86:87], 0, v[68:69]
	s_mov_b64 s[10:11], s[12:13]
	s_mov_b32 s24, s15
	global_store_dwordx4 v[86:87], v[90:93], off nt
	s_barrier
	s_cbranch_vccz .LBB0_320
